# speedup vs baseline: 1.0094x; 1.0094x over previous
.LBB0_22:
	s_or_b64 exec, exec, s[0:1]
	v_lshlrev_b64 v[20:21], 5, v[26:27]
	v_lshl_add_u64 v[20:21], v[28:29], 0, v[20:21]
	global_load_dwordx4 v[32:35], v[20:21], off nt
	global_load_dwordx4 v[36:39], v[20:21], off offset:16 nt
	s_waitcnt vmcnt(4)
	v_cvt_pk_f16_f32 v4, v4, v5
	v_cvt_pk_f16_f32 v5, v6, v7
	v_cvt_pk_f16_f32 v6, v0, v1
	v_cvt_pk_f16_f32 v7, v2, v3
	v_lshl_add_u64 v[16:17], v[16:17], 4, v[18:19]
	s_waitcnt vmcnt(2)
	v_cvt_pk_f16_f32 v0, v12, v13
	v_cvt_pk_f16_f32 v1, v14, v15
	v_cvt_pk_f16_f32 v2, v8, v9
	v_cvt_pk_f16_f32 v3, v10, v11
	v_lshl_add_u64 v[8:9], v[22:23], 4, v[24:25]
	global_store_dwordx4 v[16:17], v[4:7], off sc1
	global_store_dwordx4 v[8:9], v[0:3], off sc1
	s_nop 0
	v_lshl_add_u64 v[4:5], v[26:27], 4, v[30:31]
	s_waitcnt vmcnt(3)
	v_cvt_pk_f16_f32 v0, v32, v33
	v_cvt_pk_f16_f32 v1, v34, v35
	s_waitcnt vmcnt(2)
	v_cvt_pk_f16_f32 v2, v36, v37
	v_cvt_pk_f16_f32 v3, v38, v39
	global_store_dwordx4 v[4:5], v[0:3], off sc1
	s_endpgm
